# speedup vs baseline: 1.0330x; 1.0087x over previous
	.amdhsa_kernel _Z7dog_finPKfS0_Pf
		.amdhsa_group_segment_fixed_size 0
		.amdhsa_private_segment_fixed_size 0
		.amdhsa_kernarg_size 24
		.amdhsa_user_sgpr_count 2
		.amdhsa_user_sgpr_dispatch_ptr 0
		.amdhsa_user_sgpr_queue_ptr 0
		.amdhsa_user_sgpr_kernarg_segment_ptr 1
		.amdhsa_user_sgpr_dispatch_id 0
		.amdhsa_user_sgpr_kernarg_preload_length 0
		.amdhsa_user_sgpr_kernarg_preload_offset 0
		.amdhsa_user_sgpr_private_segment_size 0
		.amdhsa_uses_dynamic_stack 0
		.amdhsa_enable_private_segment 0
		.amdhsa_system_sgpr_workgroup_id_x 1
		.amdhsa_system_sgpr_workgroup_id_y 0
		.amdhsa_system_sgpr_workgroup_id_z 0
		.amdhsa_system_sgpr_workgroup_info 0
		.amdhsa_system_vgpr_workitem_id 0
		.amdhsa_next_free_vgpr 256
		.amdhsa_next_free_sgpr 16
		.amdhsa_accum_offset 256
		.amdhsa_reserve_vcc 1
		.amdhsa_float_round_mode_32 0
		.amdhsa_float_round_mode_16_64 0
		.amdhsa_float_denorm_mode_32 3
		.amdhsa_float_denorm_mode_16_64 3
		.amdhsa_dx10_clamp 1
		.amdhsa_ieee_mode 1
		.amdhsa_fp16_overflow 0
		.amdhsa_tg_split 0
		.amdhsa_exception_fp_ieee_invalid_op 0
		.amdhsa_exception_fp_denorm_src 0
		.amdhsa_exception_fp_ieee_div_zero 0
		.amdhsa_exception_fp_ieee_overflow 0
		.amdhsa_exception_fp_ieee_underflow 0
		.amdhsa_exception_fp_ieee_inexact 0
		.amdhsa_exception_int_div_zero 0
	.end_amdhsa_kernel

amdhsa.kernels:
  - .agpr_count:     0
    .args:
      - .address_space:  global
        .offset:         0
        .size:           8
        .value_kind:     global_buffer
      - .address_space:  global
        .offset:         8
        .size:           8
        .value_kind:     global_buffer
      - .address_space:  global
        .offset:         16
        .size:           8
        .value_kind:     global_buffer
      - .address_space:  global
        .offset:         24
        .size:           8
        .value_kind:     global_buffer
      - .address_space:  global
        .offset:         32
        .size:           8
        .value_kind:     global_buffer
      - .address_space:  global
        .offset:         40
        .size:           8
        .value_kind:     global_buffer
      - .address_space:  global
        .offset:         48
        .size:           8
        .value_kind:     global_buffer
      - .actual_access:  write_only
        .address_space:  global
        .offset:         56
        .size:           8
        .value_kind:     global_buffer
    .group_segment_fixed_size: 8704
    .kernarg_segment_align: 8
    .kernarg_segment_size: 64
    .language:       OpenCL C
    .language_version:
      - 2
      - 0
    .max_flat_workgroup_size: 512
    .name:           _Z8dog_mainPKfS0_S0_S0_S0_S0_S0_Pf
    .private_segment_fixed_size: 0
    .sgpr_count:     102
    .sgpr_spill_count: 0
    .symbol:         _Z8dog_mainPKfS0_S0_S0_S0_S0_S0_Pf.kd
    .uniform_work_group_size: 1
    .uses_dynamic_stack: false
    .vgpr_count:     256
    .vgpr_spill_count: 0
    .wavefront_size: 64
  - .agpr_count:     0
    .args:
      - .actual_access:  read_only
        .address_space:  global
        .offset:         0
        .size:           8
        .value_kind:     global_buffer
      - .actual_access:  read_only
        .address_space:  global
        .offset:         8
        .size:           8
        .value_kind:     global_buffer
      - .actual_access:  write_only
        .address_space:  global
        .offset:         16
        .size:           8
        .value_kind:     global_buffer
    .group_segment_fixed_size: 0
    .kernarg_segment_align: 8
    .kernarg_segment_size: 24
    .language:       OpenCL C
    .language_version:
      - 2
      - 0
    .max_flat_workgroup_size: 256
    .name:           _Z7dog_finPKfS0_Pf
    .private_segment_fixed_size: 0
    .sgpr_count:     16
    .sgpr_spill_count: 0
    .symbol:         _Z7dog_finPKfS0_Pf.kd
    .uniform_work_group_size: 1
    .uses_dynamic_stack: false
    .vgpr_count:     256
    .vgpr_spill_count: 0
    .wavefront_size: 64
